# i4 + phase G LN2: the two wave_sum butterflies per token via DPP adds and v_permlane16/32_swap adds instead of 12 serial ds_bpermute round trips
# baseline (speedup 1.0000x reference)
.LBB0_2910:
	s_or_b64 exec, exec, s[20:21]
	v_readlane_b32 s20, v2, 0
	s_ashr_i32 s21, s20, 31
	s_lshl_b64 s[20:21], s[20:21], 11
	v_lshl_add_u64 v[30:31], v[14:15], 0, s[20:21]
	v_readlane_b32 s20, v2, 1
	s_ashr_i32 s21, s20, 31
	s_lshl_b64 s[20:21], s[20:21], 11
	v_lshl_add_u64 v[34:35], v[14:15], 0, s[20:21]
	v_readlane_b32 s20, v2, 2
	s_ashr_i32 s21, s20, 31
	s_lshl_b64 s[20:21], s[20:21], 11
	v_lshl_add_u64 v[36:37], v[14:15], 0, s[20:21]
	v_readlane_b32 s20, v2, 3
	s_ashr_i32 s21, s20, 31
	s_lshl_b64 s[20:21], s[20:21], 11
	v_lshl_add_u64 v[38:39], v[14:15], 0, s[20:21]
	v_readlane_b32 s20, v2, 4
	s_ashr_i32 s5, s4, 31
	s_ashr_i32 s21, s20, 31
	s_lshl_b64 s[4:5], s[4:5], 12
	s_lshl_b64 s[20:21], s[20:21], 11
	v_lshl_add_u64 v[12:13], v[16:17], 0, s[4:5]
	v_lshl_add_u64 v[28:29], v[18:19], 0, s[4:5]
	global_load_dwordx2 v[32:33], v[30:31], off
	global_load_dwordx2 v[98:99], v[34:35], off
	global_load_dwordx2 v[62:63], v[36:37], off
	global_load_dwordx2 v[68:69], v[38:39], off
	v_lshl_add_u64 v[40:41], v[14:15], 0, s[20:21]
	v_readlane_b32 s20, v2, 5
	global_load_dwordx4 v[76:79], v[12:13], off
	global_load_dwordx4 v[94:97], v[28:29], off
	s_ashr_i32 s21, s20, 31
	s_lshl_b64 s[20:21], s[20:21], 11
	v_lshl_add_u64 v[42:43], v[14:15], 0, s[20:21]
	v_readlane_b32 s20, v2, 6
	s_ashr_i32 s21, s20, 31
	global_load_dwordx2 v[70:71], v[40:41], off
	global_load_dwordx2 v[72:73], v[42:43], off
	s_lshl_b64 s[20:21], s[20:21], 11
	v_lshl_add_u64 v[44:45], v[14:15], 0, s[20:21]
	global_load_dwordx2 v[74:75], v[44:45], off
	v_readlane_b32 s20, v2, 7
	s_ashr_i32 s21, s20, 31
	s_lshl_b64 s[20:21], s[20:21], 11
	v_lshl_add_u64 v[46:47], v[14:15], 0, s[20:21]
	global_load_dwordx2 v[88:89], v[46:47], off
	global_load_dwordx4 v[4:7], v[12:13], off offset:1024
	global_load_dwordx4 v[8:11], v[28:29], off offset:1024
	global_load_dwordx2 v[66:67], v[30:31], off offset:512
	global_load_dwordx2 v[64:65], v[34:35], off offset:512
	global_load_dwordx2 v[60:61], v[36:37], off offset:512
	global_load_dwordx2 v[56:57], v[38:39], off offset:512
	global_load_dwordx2 v[54:55], v[40:41], off offset:512
	global_load_dwordx2 v[52:53], v[42:43], off offset:512
	global_load_dwordx2 v[50:51], v[44:45], off offset:512
	global_load_dwordx2 v[48:49], v[46:47], off offset:512
	v_readlane_b32 s5, v1, 0
	s_mov_b32 s4, 0
	s_waitcnt vmcnt(10) lgkmcnt(0)
	v_cvt_pk_f32_fp8_e32 v[112:113], v32
	v_cvt_pk_f32_fp8_sdwa v[100:101], v32 src0_sel:WORD_1
	v_cvt_pk_f32_fp8_e32 v[114:115], v98
	v_cvt_pk_f32_fp8_sdwa v[116:117], v98 src0_sel:WORD_1
	v_cvt_pk_f32_fp8_e32 v[118:119], v99
	v_cvt_pk_f32_fp8_sdwa v[98:99], v99 src0_sel:WORD_1
	v_lshlrev_b32_e32 v90, 16, v76
	v_lshlrev_b32_e32 v92, 16, v94
	v_and_b32_e32 v91, 0xffff0000, v76
	v_and_b32_e32 v93, 0xffff0000, v94
	v_lshlrev_b32_e32 v84, 16, v77
	v_lshlrev_b32_e32 v86, 16, v95
	v_and_b32_e32 v85, 0xffff0000, v77
	v_and_b32_e32 v87, 0xffff0000, v95
	v_lshlrev_b32_e32 v80, 16, v78
	v_lshlrev_b32_e32 v82, 16, v96
	v_and_b32_e32 v81, 0xffff0000, v78
	v_and_b32_e32 v83, 0xffff0000, v96
	v_lshlrev_b32_e32 v76, 16, v79
	v_lshlrev_b32_e32 v78, 16, v97
	v_and_b32_e32 v77, 0xffff0000, v79
	v_and_b32_e32 v79, 0xffff0000, v97
	v_cvt_pk_f32_fp8_e32 v[96:97], v33
	v_cvt_pk_f32_fp8_sdwa v[94:95], v33 src0_sel:WORD_1
	v_cvt_pk_f32_fp8_e32 v[120:121], v62
	v_cvt_pk_f32_fp8_sdwa v[122:123], v62 src0_sel:WORD_1
	v_mul_f32_e32 v2, s5, v225
	v_readlane_b32 s5, v1, 1
	v_cvt_pk_f32_fp8_e32 v[124:125], v63
	v_cvt_pk_f32_fp8_sdwa v[126:127], v63 src0_sel:WORD_1
	v_cvt_pk_f32_fp8_e32 v[128:129], v68
	v_cvt_pk_f32_fp8_e32 v[160:161], v88
	v_cvt_pk_f32_fp8_sdwa v[162:163], v88 src0_sel:WORD_1
	v_cvt_pk_f32_fp8_e32 v[164:165], v89
	v_cvt_pk_f32_fp8_sdwa v[166:167], v89 src0_sel:WORD_1
	v_pk_fma_f32 v[88:89], v[90:91], s[96:97], v[92:93] op_sel_hi:[1,0,1]
	v_pk_fma_f32 v[84:85], v[84:85], s[96:97], v[86:87] op_sel_hi:[1,0,1]
	v_mul_f32_e32 v32, s5, v225
	v_readlane_b32 s5, v1, 2
	v_cvt_pk_f32_fp8_sdwa v[130:131], v68 src0_sel:WORD_1
	v_cvt_pk_f32_fp8_e32 v[132:133], v69
	v_cvt_pk_f32_fp8_sdwa v[134:135], v69 src0_sel:WORD_1
	v_pk_fma_f32 v[88:89], v[2:3], v[112:113], v[88:89] op_sel_hi:[0,1,1]
	v_pk_fma_f32 v[84:85], v[2:3], v[100:101], v[84:85] op_sel_hi:[0,1,1]
	v_pk_fma_f32 v[80:81], v[80:81], s[96:97], v[82:83] op_sel_hi:[1,0,1]
	v_pk_fma_f32 v[76:77], v[76:77], s[96:97], v[78:79] op_sel_hi:[1,0,1]
	v_mul_f32_e32 v58, s5, v225
	v_readlane_b32 s5, v1, 3
	v_cvt_pk_f32_fp8_e32 v[136:137], v70
	v_cvt_pk_f32_fp8_sdwa v[138:139], v70 src0_sel:WORD_1
	v_cvt_pk_f32_fp8_e32 v[140:141], v71
	v_pk_fma_f32 v[88:89], v[32:33], v[114:115], v[88:89] op_sel_hi:[0,1,1]
	v_pk_fma_f32 v[84:85], v[32:33], v[116:117], v[84:85] op_sel_hi:[0,1,1]
	v_pk_fma_f32 v[80:81], v[2:3], v[96:97], v[80:81] op_sel_hi:[0,1,1]
	v_pk_fma_f32 v[76:77], v[2:3], v[94:95], v[76:77] op_sel_hi:[0,1,1]
	v_mul_f32_e32 v62, s5, v225
	v_cvt_pk_f32_fp8_sdwa v[142:143], v71 src0_sel:WORD_1
	v_cvt_pk_f32_fp8_e32 v[144:145], v72
	v_cvt_pk_f32_fp8_sdwa v[146:147], v72 src0_sel:WORD_1
	v_pk_fma_f32 v[88:89], v[58:59], v[120:121], v[88:89] op_sel_hi:[0,1,1]
	v_pk_fma_f32 v[84:85], v[58:59], v[122:123], v[84:85] op_sel_hi:[0,1,1]
	v_pk_fma_f32 v[80:81], v[32:33], v[118:119], v[80:81] op_sel_hi:[0,1,1]
	v_pk_fma_f32 v[76:77], v[32:33], v[98:99], v[76:77] op_sel_hi:[0,1,1]
	s_waitcnt vmcnt(0)
	v_lshlrev_b32_e32 v120, 16, v10
	v_and_b32_e32 v121, 0xffff0000, v10
	v_lshlrev_b32_e32 v122, 16, v11
	v_and_b32_e32 v123, 0xffff0000, v11
	v_cvt_pk_f32_fp8_sdwa v[10:11], v66 src0_sel:WORD_1
	v_readlane_b32 s5, v1, 4
	v_cvt_pk_f32_fp8_e32 v[148:149], v73
	v_cvt_pk_f32_fp8_sdwa v[150:151], v73 src0_sel:WORD_1
	v_cvt_pk_f32_fp8_e32 v[152:153], v74
	v_pk_fma_f32 v[88:89], v[62:63], v[128:129], v[88:89] op_sel_hi:[0,1,1]
	v_pk_fma_f32 v[80:81], v[58:59], v[124:125], v[80:81] op_sel_hi:[0,1,1]
	v_pk_fma_f32 v[76:77], v[58:59], v[126:127], v[76:77] op_sel_hi:[0,1,1]
	v_cvt_pk_f32_fp8_sdwa v[128:129], v64 src0_sel:WORD_1
	v_mul_f32_e32 v68, s5, v225
	v_readlane_b32 s5, v1, 5
	v_cvt_pk_f32_fp8_e32 v[156:157], v75
	v_cvt_pk_f32_fp8_sdwa v[158:159], v75 src0_sel:WORD_1
	v_pk_fma_f32 v[84:85], v[62:63], v[130:131], v[84:85] op_sel_hi:[0,1,1]
	v_pk_fma_f32 v[80:81], v[62:63], v[132:133], v[80:81] op_sel_hi:[0,1,1]
	v_pk_fma_f32 v[76:77], v[62:63], v[134:135], v[76:77] op_sel_hi:[0,1,1]
	v_lshlrev_b32_e32 v112, 16, v4
	v_and_b32_e32 v113, 0xffff0000, v4
	v_lshlrev_b32_e32 v4, 16, v5
	v_lshlrev_b32_e32 v116, 16, v9
	v_and_b32_e32 v5, 0xffff0000, v5
	v_and_b32_e32 v117, 0xffff0000, v9
	v_cvt_pk_f32_fp8_sdwa v[134:135], v60 src0_sel:WORD_1
	v_mul_f32_e32 v70, s5, v225
	v_readlane_b32 s5, v1, 6
	v_pk_fma_f32 v[88:89], v[68:69], v[136:137], v[88:89] op_sel_hi:[0,1,1]
	v_pk_fma_f32 v[84:85], v[68:69], v[138:139], v[84:85] op_sel_hi:[0,1,1]
	v_pk_fma_f32 v[80:81], v[68:69], v[140:141], v[80:81] op_sel_hi:[0,1,1]
	v_cvt_pk_f32_fp8_sdwa v[140:141], v56 src0_sel:WORD_1
	v_pk_fma_f32 v[4:5], v[4:5], s[96:97], v[116:117] op_sel_hi:[1,0,1]
	v_mul_f32_e32 v72, s5, v225
	v_pk_fma_f32 v[88:89], v[70:71], v[144:145], v[88:89] op_sel_hi:[0,1,1]
	v_pk_fma_f32 v[84:85], v[70:71], v[146:147], v[84:85] op_sel_hi:[0,1,1]
	v_pk_fma_f32 v[76:77], v[68:69], v[142:143], v[76:77] op_sel_hi:[0,1,1]
	v_cvt_pk_f32_fp8_sdwa v[146:147], v54 src0_sel:WORD_1
	v_pk_fma_f32 v[4:5], v[2:3], v[10:11], v[4:5] op_sel_hi:[0,1,1]
	v_readlane_b32 s5, v1, 7
	v_pk_fma_f32 v[88:89], v[72:73], v[152:153], v[88:89] op_sel_hi:[0,1,1]
	v_pk_fma_f32 v[80:81], v[70:71], v[148:149], v[80:81] op_sel_hi:[0,1,1]
	v_pk_fma_f32 v[76:77], v[70:71], v[150:151], v[76:77] op_sel_hi:[0,1,1]
	v_cvt_pk_f32_fp8_sdwa v[152:153], v52 src0_sel:WORD_1
	v_pk_fma_f32 v[4:5], v[32:33], v[128:129], v[4:5] op_sel_hi:[0,1,1]
	v_cvt_pk_f32_fp8_sdwa v[154:155], v74 src0_sel:WORD_1
	v_mul_f32_e32 v74, s5, v225
	v_pk_fma_f32 v[80:81], v[72:73], v[156:157], v[80:81] op_sel_hi:[0,1,1]
	v_pk_fma_f32 v[76:77], v[72:73], v[158:159], v[76:77] op_sel_hi:[0,1,1]
	v_cvt_pk_f32_fp8_sdwa v[158:159], v50 src0_sel:WORD_1
	v_pk_fma_f32 v[4:5], v[58:59], v[134:135], v[4:5] op_sel_hi:[0,1,1]
	v_pk_fma_f32 v[80:81], v[74:75], v[164:165], v[80:81] op_sel_hi:[0,1,1]
	v_cvt_pk_f32_fp8_sdwa v[164:165], v48 src0_sel:WORD_1
	v_pk_fma_f32 v[4:5], v[62:63], v[140:141], v[4:5] op_sel_hi:[0,1,1]
	v_cvt_pk_f32_fp8_e32 v[124:125], v67
	v_pk_fma_f32 v[4:5], v[68:69], v[146:147], v[4:5] op_sel_hi:[0,1,1]
	v_cvt_pk_f32_fp8_e32 v[130:131], v65
	v_pk_fma_f32 v[4:5], v[70:71], v[152:153], v[4:5] op_sel_hi:[0,1,1]
	v_lshlrev_b32_e32 v118, 16, v6
	v_and_b32_e32 v119, 0xffff0000, v6
	v_cvt_pk_f32_fp8_e32 v[136:137], v61
	v_pk_fma_f32 v[4:5], v[72:73], v[158:159], v[4:5] op_sel_hi:[0,1,1]
	v_cvt_pk_f32_fp8_e32 v[142:143], v57
	v_pk_fma_f32 v[10:11], v[74:75], v[164:165], v[4:5] op_sel_hi:[0,1,1]
	v_pk_fma_f32 v[4:5], v[118:119], s[96:97], v[120:121] op_sel_hi:[1,0,1]
	v_cvt_pk_f32_fp8_e32 v[148:149], v55
	v_pk_fma_f32 v[4:5], v[2:3], v[124:125], v[4:5] op_sel_hi:[0,1,1]
	v_pk_fma_f32 v[88:89], v[74:75], v[160:161], v[88:89] op_sel_hi:[0,1,1]
	v_pk_fma_f32 v[84:85], v[72:73], v[154:155], v[84:85] op_sel_hi:[0,1,1]
	v_cvt_pk_f32_fp8_e32 v[154:155], v53
	v_pk_fma_f32 v[4:5], v[32:33], v[130:131], v[4:5] op_sel_hi:[0,1,1]
	v_pk_fma_f32 v[90:91], v[74:75], v[162:163], v[84:85] op_sel_hi:[0,1,1]
	v_pk_fma_f32 v[82:83], v[74:75], v[166:167], v[76:77] op_sel_hi:[0,1,1]
	v_mov_b32_e32 v76, v88
	v_mov_b32_e32 v77, v80
	v_mov_b32_e32 v78, v89
	v_mov_b32_e32 v79, v81
	v_cvt_pk_f32_fp8_e32 v[160:161], v51
	v_pk_fma_f32 v[4:5], v[58:59], v[136:137], v[4:5] op_sel_hi:[0,1,1]
	v_pk_add_f32 v[76:77], v[76:77], v[78:79]
	v_mov_b32_e32 v78, v90
	v_mov_b32_e32 v79, v82
	v_mov_b32_e32 v84, v91
	v_mov_b32_e32 v85, v83
	v_lshlrev_b32_e32 v114, 16, v8
	v_and_b32_e32 v115, 0xffff0000, v8
	v_cvt_pk_f32_fp8_e32 v[8:9], v66
	v_cvt_pk_f32_fp8_e32 v[166:167], v49
	v_pk_fma_f32 v[4:5], v[62:63], v[142:143], v[4:5] op_sel_hi:[0,1,1]
	v_pk_add_f32 v[78:79], v[78:79], v[84:85]
	ds_write_b128 v103, v[88:91]
	ds_write_b128 v103, v[80:83] offset:16
	v_cvt_pk_f32_fp8_sdwa v[66:67], v67 src0_sel:WORD_1
	v_cvt_pk_f32_fp8_e32 v[126:127], v64
	v_pk_fma_f32 v[4:5], v[68:69], v[148:149], v[4:5] op_sel_hi:[0,1,1]
	v_pk_add_f32 v[76:77], v[76:77], v[78:79]
	global_load_dwordx4 v[78:81], v[12:13], off offset:2048
	global_load_dwordx4 v[82:85], v[28:29], off offset:2048
	global_load_dwordx2 v[86:87], v[30:31], off offset:1024
	global_load_dwordx2 v[88:89], v[34:35], off offset:1024
	global_load_dwordx2 v[90:91], v[36:37], off offset:1024
	global_load_dwordx2 v[92:93], v[38:39], off offset:1024
	global_load_dwordx2 v[94:95], v[40:41], off offset:1024
	global_load_dwordx2 v[96:97], v[42:43], off offset:1024
	global_load_dwordx2 v[98:99], v[44:45], off offset:1024
	global_load_dwordx2 v[100:101], v[46:47], off offset:1024
	v_cvt_pk_f32_fp8_sdwa v[64:65], v65 src0_sel:WORD_1
	v_cvt_pk_f32_fp8_e32 v[132:133], v60
	v_pk_fma_f32 v[4:5], v[70:71], v[154:155], v[4:5] op_sel_hi:[0,1,1]
	v_lshlrev_b32_e32 v6, 16, v7
	v_and_b32_e32 v7, 0xffff0000, v7
	v_cvt_pk_f32_fp8_sdwa v[60:61], v61 src0_sel:WORD_1
	v_cvt_pk_f32_fp8_e32 v[138:139], v56
	v_cvt_pk_f32_fp8_e32 v[162:163], v48
	v_cvt_pk_f32_fp8_sdwa v[168:169], v49 src0_sel:WORD_1
	v_pk_fma_f32 v[48:49], v[112:113], s[96:97], v[114:115] op_sel_hi:[1,0,1]
	v_pk_fma_f32 v[4:5], v[72:73], v[160:161], v[4:5] op_sel_hi:[0,1,1]
	v_cvt_pk_f32_fp8_sdwa v[56:57], v57 src0_sel:WORD_1
	v_cvt_pk_f32_fp8_e32 v[144:145], v54
	v_pk_fma_f32 v[8:9], v[2:3], v[8:9], v[48:49] op_sel_hi:[0,1,1]
	v_pk_fma_f32 v[48:49], v[74:75], v[166:167], v[4:5] op_sel_hi:[0,1,1]
	v_pk_fma_f32 v[4:5], v[6:7], s[96:97], v[122:123] op_sel_hi:[1,0,1]
	v_cvt_pk_f32_fp8_sdwa v[54:55], v55 src0_sel:WORD_1
	v_cvt_pk_f32_fp8_e32 v[150:151], v52
	v_pk_fma_f32 v[8:9], v[32:33], v[126:127], v[8:9] op_sel_hi:[0,1,1]
	v_pk_fma_f32 v[4:5], v[2:3], v[66:67], v[4:5] op_sel_hi:[0,1,1]
	v_cvt_pk_f32_fp8_sdwa v[52:53], v53 src0_sel:WORD_1
	v_cvt_pk_f32_fp8_e32 v[156:157], v50
	v_pk_fma_f32 v[8:9], v[58:59], v[132:133], v[8:9] op_sel_hi:[0,1,1]
	v_pk_fma_f32 v[4:5], v[32:33], v[64:65], v[4:5] op_sel_hi:[0,1,1]
	v_cvt_pk_f32_fp8_sdwa v[50:51], v51 src0_sel:WORD_1
	v_pk_fma_f32 v[8:9], v[62:63], v[138:139], v[8:9] op_sel_hi:[0,1,1]
	v_pk_fma_f32 v[4:5], v[58:59], v[60:61], v[4:5] op_sel_hi:[0,1,1]
	v_pk_fma_f32 v[8:9], v[68:69], v[144:145], v[8:9] op_sel_hi:[0,1,1]
	v_pk_fma_f32 v[4:5], v[62:63], v[56:57], v[4:5] op_sel_hi:[0,1,1]
	v_pk_fma_f32 v[8:9], v[70:71], v[150:151], v[8:9] op_sel_hi:[0,1,1]
	v_pk_fma_f32 v[4:5], v[68:69], v[54:55], v[4:5] op_sel_hi:[0,1,1]
	v_pk_fma_f32 v[8:9], v[72:73], v[156:157], v[8:9] op_sel_hi:[0,1,1]
	v_pk_fma_f32 v[4:5], v[70:71], v[52:53], v[4:5] op_sel_hi:[0,1,1]
	v_pk_fma_f32 v[8:9], v[74:75], v[162:163], v[8:9] op_sel_hi:[0,1,1]
	v_pk_fma_f32 v[4:5], v[72:73], v[50:51], v[4:5] op_sel_hi:[0,1,1]
	v_pk_fma_f32 v[50:51], v[74:75], v[168:169], v[4:5] op_sel_hi:[0,1,1]
	v_mov_b32_e32 v4, v8
	v_mov_b32_e32 v5, v10
	v_mov_b32_e32 v6, v9
	v_mov_b32_e32 v7, v11
	v_pk_add_f32 v[4:5], v[4:5], v[6:7]
	v_mov_b32_e32 v6, v48
	v_mov_b32_e32 v7, v50
	v_mov_b32_e32 v52, v49
	v_mov_b32_e32 v53, v51
	ds_write_b128 v103, v[8:11] offset:2048
	ds_write_b128 v103, v[48:51] offset:2064
	v_pk_add_f32 v[6:7], v[6:7], v[52:53]
	global_load_dwordx4 v[8:11], v[12:13], off offset:3072
	global_load_dwordx4 v[48:51], v[28:29], off offset:3072
	s_nop 0
	global_load_dwordx2 v[12:13], v[30:31], off offset:1536
	global_load_dwordx2 v[52:53], v[34:35], off offset:1536
	global_load_dwordx2 v[54:55], v[36:37], off offset:1536
	s_nop 0
	global_load_dwordx2 v[38:39], v[38:39], off offset:1536
	s_nop 0
	global_load_dwordx2 v[40:41], v[40:41], off offset:1536
	s_nop 0
	global_load_dwordx2 v[42:43], v[42:43], off offset:1536
	s_nop 0
	global_load_dwordx2 v[44:45], v[44:45], off offset:1536
	s_nop 0
	global_load_dwordx2 v[46:47], v[46:47], off offset:1536
	v_pk_add_f32 v[76:77], v[76:77], v[76:77] op_sel:[0,1] op_sel_hi:[1,0]
	v_pk_add_f32 v[4:5], v[4:5], v[4:5] op_sel:[0,1] op_sel_hi:[1,0]
	v_pk_add_f32 v[6:7], v[6:7], v[6:7] op_sel:[0,1] op_sel_hi:[1,0]
	s_waitcnt vmcnt(10) lgkmcnt(0)
	v_lshlrev_b32_e32 v28, 16, v78
	v_lshlrev_b32_e32 v30, 16, v82
	v_and_b32_e32 v29, 0xffff0000, v78
	v_and_b32_e32 v31, 0xffff0000, v82
	v_lshlrev_b32_e32 v34, 16, v79
	v_lshlrev_b32_e32 v36, 16, v83
	v_and_b32_e32 v35, 0xffff0000, v79
	v_and_b32_e32 v37, 0xffff0000, v83
	v_lshlrev_b32_e32 v56, 16, v80
	v_and_b32_e32 v57, 0xffff0000, v80
	v_lshlrev_b32_e32 v64, 16, v81
	v_and_b32_e32 v65, 0xffff0000, v81
	v_cvt_pk_f32_fp8_e32 v[78:79], v86
	v_cvt_pk_f32_fp8_sdwa v[80:81], v86 src0_sel:WORD_1
	v_cvt_pk_f32_fp8_e32 v[82:83], v87
	v_lshlrev_b32_e32 v60, 16, v84
	v_and_b32_e32 v61, 0xffff0000, v84
	v_lshlrev_b32_e32 v66, 16, v85
	v_and_b32_e32 v67, 0xffff0000, v85
	v_cvt_pk_f32_fp8_sdwa v[84:85], v87 src0_sel:WORD_1
	v_cvt_pk_f32_fp8_e32 v[86:87], v88
	v_cvt_pk_f32_fp8_sdwa v[112:113], v88 src0_sel:WORD_1
	v_cvt_pk_f32_fp8_e32 v[114:115], v89
	v_cvt_pk_f32_fp8_sdwa v[88:89], v89 src0_sel:WORD_1
	v_cvt_pk_f32_fp8_e32 v[116:117], v90
	v_cvt_pk_f32_fp8_sdwa v[118:119], v90 src0_sel:WORD_1
	v_cvt_pk_f32_fp8_e32 v[120:121], v91
	v_cvt_pk_f32_fp8_sdwa v[90:91], v91 src0_sel:WORD_1
	v_cvt_pk_f32_fp8_e32 v[122:123], v92
	v_cvt_pk_f32_fp8_sdwa v[124:125], v92 src0_sel:WORD_1
	v_cvt_pk_f32_fp8_e32 v[126:127], v93
	v_pk_fma_f32 v[28:29], v[28:29], s[96:97], v[30:31] op_sel_hi:[1,0,1]
	v_pk_fma_f32 v[30:31], v[34:35], s[96:97], v[36:37] op_sel_hi:[1,0,1]
	v_pk_fma_f32 v[34:35], v[56:57], s[96:97], v[60:61] op_sel_hi:[1,0,1]
	v_cvt_pk_f32_fp8_sdwa v[92:93], v93 src0_sel:WORD_1
	v_cvt_pk_f32_fp8_e32 v[128:129], v94
	v_cvt_pk_f32_fp8_sdwa v[130:131], v94 src0_sel:WORD_1
	v_cvt_pk_f32_fp8_e32 v[132:133], v95
	v_pk_fma_f32 v[28:29], v[2:3], v[78:79], v[28:29] op_sel_hi:[0,1,1]
	v_pk_fma_f32 v[30:31], v[2:3], v[80:81], v[30:31] op_sel_hi:[0,1,1]
	v_pk_fma_f32 v[34:35], v[2:3], v[82:83], v[34:35] op_sel_hi:[0,1,1]
	v_pk_fma_f32 v[36:37], v[64:65], s[96:97], v[66:67] op_sel_hi:[1,0,1]
	v_cvt_pk_f32_fp8_sdwa v[94:95], v95 src0_sel:WORD_1
	v_cvt_pk_f32_fp8_e32 v[134:135], v96
	v_cvt_pk_f32_fp8_sdwa v[136:137], v96 src0_sel:WORD_1
	v_cvt_pk_f32_fp8_e32 v[138:139], v97
	v_pk_fma_f32 v[28:29], v[32:33], v[86:87], v[28:29] op_sel_hi:[0,1,1]
	v_pk_fma_f32 v[30:31], v[32:33], v[112:113], v[30:31] op_sel_hi:[0,1,1]
	v_pk_fma_f32 v[34:35], v[32:33], v[114:115], v[34:35] op_sel_hi:[0,1,1]
	v_pk_fma_f32 v[36:37], v[2:3], v[84:85], v[36:37] op_sel_hi:[0,1,1]
	v_cvt_pk_f32_fp8_sdwa v[96:97], v97 src0_sel:WORD_1
	v_cvt_pk_f32_fp8_e32 v[140:141], v98
	v_cvt_pk_f32_fp8_sdwa v[142:143], v98 src0_sel:WORD_1
	v_cvt_pk_f32_fp8_e32 v[144:145], v99
	v_pk_fma_f32 v[28:29], v[58:59], v[116:117], v[28:29] op_sel_hi:[0,1,1]
	v_pk_fma_f32 v[30:31], v[58:59], v[118:119], v[30:31] op_sel_hi:[0,1,1]
	v_pk_fma_f32 v[34:35], v[58:59], v[120:121], v[34:35] op_sel_hi:[0,1,1]
	v_pk_fma_f32 v[36:37], v[32:33], v[88:89], v[36:37] op_sel_hi:[0,1,1]
	v_cvt_pk_f32_fp8_sdwa v[98:99], v99 src0_sel:WORD_1
	v_cvt_pk_f32_fp8_e32 v[146:147], v100
	v_cvt_pk_f32_fp8_sdwa v[148:149], v100 src0_sel:WORD_1
	v_cvt_pk_f32_fp8_e32 v[150:151], v101
	v_pk_fma_f32 v[28:29], v[62:63], v[122:123], v[28:29] op_sel_hi:[0,1,1]
	v_pk_fma_f32 v[30:31], v[62:63], v[124:125], v[30:31] op_sel_hi:[0,1,1]
	v_pk_fma_f32 v[34:35], v[62:63], v[126:127], v[34:35] op_sel_hi:[0,1,1]
	v_pk_fma_f32 v[36:37], v[58:59], v[90:91], v[36:37] op_sel_hi:[0,1,1]
	v_cvt_pk_f32_fp8_sdwa v[100:101], v101 src0_sel:WORD_1
	v_pk_fma_f32 v[28:29], v[68:69], v[128:129], v[28:29] op_sel_hi:[0,1,1]
	v_pk_fma_f32 v[30:31], v[68:69], v[130:131], v[30:31] op_sel_hi:[0,1,1]
	v_pk_fma_f32 v[34:35], v[68:69], v[132:133], v[34:35] op_sel_hi:[0,1,1]
	v_pk_fma_f32 v[36:37], v[62:63], v[92:93], v[36:37] op_sel_hi:[0,1,1]
	v_pk_fma_f32 v[28:29], v[70:71], v[134:135], v[28:29] op_sel_hi:[0,1,1]
	v_pk_fma_f32 v[30:31], v[70:71], v[136:137], v[30:31] op_sel_hi:[0,1,1]
	v_pk_fma_f32 v[34:35], v[70:71], v[138:139], v[34:35] op_sel_hi:[0,1,1]
	v_pk_fma_f32 v[36:37], v[68:69], v[94:95], v[36:37] op_sel_hi:[0,1,1]
	v_pk_fma_f32 v[28:29], v[72:73], v[140:141], v[28:29] op_sel_hi:[0,1,1]
	v_pk_fma_f32 v[30:31], v[72:73], v[142:143], v[30:31] op_sel_hi:[0,1,1]
	v_pk_fma_f32 v[34:35], v[72:73], v[144:145], v[34:35] op_sel_hi:[0,1,1]
	v_pk_fma_f32 v[36:37], v[70:71], v[96:97], v[36:37] op_sel_hi:[0,1,1]
	v_pk_fma_f32 v[28:29], v[74:75], v[146:147], v[28:29] op_sel_hi:[0,1,1]
	v_pk_fma_f32 v[30:31], v[74:75], v[148:149], v[30:31] op_sel_hi:[0,1,1]
	v_pk_fma_f32 v[34:35], v[74:75], v[150:151], v[34:35] op_sel_hi:[0,1,1]
	v_pk_fma_f32 v[36:37], v[72:73], v[98:99], v[36:37] op_sel_hi:[0,1,1]
	v_pk_fma_f32 v[36:37], v[74:75], v[100:101], v[36:37] op_sel_hi:[0,1,1]
	v_pk_add_f32 v[56:57], v[28:29], v[28:29] op_sel:[1,0] op_sel_hi:[0,1]
	v_pk_add_f32 v[64:65], v[34:35], v[34:35] op_sel:[1,0] op_sel_hi:[0,1]
	ds_write_b128 v103, v[28:31] offset:4096
	ds_write_b128 v103, v[34:37] offset:4112
	s_waitcnt vmcnt(0)
	v_lshlrev_b32_e32 v28, 16, v8
	v_and_b32_e32 v29, 0xffff0000, v8
	v_lshlrev_b32_e32 v34, 16, v9
	v_and_b32_e32 v35, 0xffff0000, v9
	v_cvt_pk_f32_fp8_e32 v[8:9], v12
	v_pk_add_f32 v[60:61], v[30:31], v[30:31] op_sel:[1,0] op_sel_hi:[0,1]
	v_pk_add_f32 v[66:67], v[36:37], v[36:37] op_sel:[1,0] op_sel_hi:[0,1]
	v_lshlrev_b32_e32 v30, 16, v48
	v_and_b32_e32 v31, 0xffff0000, v48
	v_lshlrev_b32_e32 v36, 16, v49
	v_and_b32_e32 v37, 0xffff0000, v49
	v_lshlrev_b32_e32 v48, 16, v10
	v_and_b32_e32 v49, 0xffff0000, v10
	v_lshlrev_b32_e32 v80, 16, v11
	v_and_b32_e32 v81, 0xffff0000, v11
	v_cvt_pk_f32_fp8_sdwa v[10:11], v12 src0_sel:WORD_1
	v_cvt_pk_f32_fp8_e32 v[82:83], v13
	v_cvt_pk_f32_fp8_sdwa v[12:13], v13 src0_sel:WORD_1
	v_cvt_pk_f32_fp8_e32 v[84:85], v52
	v_cvt_pk_f32_fp8_sdwa v[86:87], v52 src0_sel:WORD_1
	v_cvt_pk_f32_fp8_e32 v[88:89], v53
	v_cvt_pk_f32_fp8_sdwa v[52:53], v53 src0_sel:WORD_1
	v_cvt_pk_f32_fp8_e32 v[90:91], v54
	v_cvt_pk_f32_fp8_sdwa v[92:93], v54 src0_sel:WORD_1
	v_pk_fma_f32 v[28:29], v[28:29], s[96:97], v[30:31] op_sel_hi:[1,0,1]
	v_lshlrev_b32_e32 v78, 16, v50
	v_and_b32_e32 v79, 0xffff0000, v50
	v_lshlrev_b32_e32 v50, 16, v51
	v_and_b32_e32 v51, 0xffff0000, v51
	v_cvt_pk_f32_fp8_e32 v[94:95], v55
	v_cvt_pk_f32_fp8_sdwa v[54:55], v55 src0_sel:WORD_1
	v_cvt_pk_f32_fp8_e32 v[96:97], v38
	v_cvt_pk_f32_fp8_sdwa v[98:99], v38 src0_sel:WORD_1
	v_pk_fma_f32 v[8:9], v[2:3], v[8:9], v[28:29] op_sel_hi:[0,1,1]
	v_pk_fma_f32 v[28:29], v[34:35], s[96:97], v[36:37] op_sel_hi:[1,0,1]
	v_cvt_pk_f32_fp8_e32 v[100:101], v39
	v_cvt_pk_f32_fp8_sdwa v[38:39], v39 src0_sel:WORD_1
	v_cvt_pk_f32_fp8_e32 v[112:113], v40
	v_cvt_pk_f32_fp8_sdwa v[114:115], v40 src0_sel:WORD_1
	v_pk_fma_f32 v[10:11], v[2:3], v[10:11], v[28:29] op_sel_hi:[0,1,1]
	v_pk_fma_f32 v[28:29], v[48:49], s[96:97], v[78:79] op_sel_hi:[1,0,1]
	v_pk_fma_f32 v[30:31], v[80:81], s[96:97], v[50:51] op_sel_hi:[1,0,1]
	v_cvt_pk_f32_fp8_e32 v[116:117], v41
	v_cvt_pk_f32_fp8_sdwa v[40:41], v41 src0_sel:WORD_1
	v_cvt_pk_f32_fp8_e32 v[118:119], v42
	v_cvt_pk_f32_fp8_sdwa v[120:121], v42 src0_sel:WORD_1
	v_pk_fma_f32 v[8:9], v[32:33], v[84:85], v[8:9] op_sel_hi:[0,1,1]
	v_pk_fma_f32 v[10:11], v[32:33], v[86:87], v[10:11] op_sel_hi:[0,1,1]
	v_pk_fma_f32 v[28:29], v[2:3], v[82:83], v[28:29] op_sel_hi:[0,1,1]
	v_pk_fma_f32 v[12:13], v[2:3], v[12:13], v[30:31] op_sel_hi:[0,1,1]
	v_cvt_pk_f32_fp8_e32 v[122:123], v43
	v_cvt_pk_f32_fp8_sdwa v[42:43], v43 src0_sel:WORD_1
	v_cvt_pk_f32_fp8_e32 v[124:125], v44
	v_cvt_pk_f32_fp8_sdwa v[126:127], v44 src0_sel:WORD_1
	v_pk_fma_f32 v[8:9], v[58:59], v[90:91], v[8:9] op_sel_hi:[0,1,1]
	v_pk_fma_f32 v[10:11], v[58:59], v[92:93], v[10:11] op_sel_hi:[0,1,1]
	v_pk_fma_f32 v[28:29], v[32:33], v[88:89], v[28:29] op_sel_hi:[0,1,1]
	v_pk_fma_f32 v[12:13], v[32:33], v[52:53], v[12:13] op_sel_hi:[0,1,1]
	v_cvt_pk_f32_fp8_e32 v[128:129], v45
	v_cvt_pk_f32_fp8_sdwa v[44:45], v45 src0_sel:WORD_1
	v_cvt_pk_f32_fp8_e32 v[130:131], v46
	v_cvt_pk_f32_fp8_sdwa v[132:133], v46 src0_sel:WORD_1
	v_pk_fma_f32 v[8:9], v[62:63], v[96:97], v[8:9] op_sel_hi:[0,1,1]
	v_pk_fma_f32 v[10:11], v[62:63], v[98:99], v[10:11] op_sel_hi:[0,1,1]
	v_pk_fma_f32 v[28:29], v[58:59], v[94:95], v[28:29] op_sel_hi:[0,1,1]
	v_pk_fma_f32 v[12:13], v[58:59], v[54:55], v[12:13] op_sel_hi:[0,1,1]
	v_cvt_pk_f32_fp8_e32 v[134:135], v47
	v_cvt_pk_f32_fp8_sdwa v[46:47], v47 src0_sel:WORD_1
	v_pk_fma_f32 v[8:9], v[68:69], v[112:113], v[8:9] op_sel_hi:[0,1,1]
	v_pk_fma_f32 v[10:11], v[68:69], v[114:115], v[10:11] op_sel_hi:[0,1,1]
	v_pk_fma_f32 v[28:29], v[62:63], v[100:101], v[28:29] op_sel_hi:[0,1,1]
	v_pk_fma_f32 v[12:13], v[62:63], v[38:39], v[12:13] op_sel_hi:[0,1,1]
	v_pk_fma_f32 v[8:9], v[70:71], v[118:119], v[8:9] op_sel_hi:[0,1,1]
	v_pk_fma_f32 v[10:11], v[70:71], v[120:121], v[10:11] op_sel_hi:[0,1,1]
	v_pk_fma_f32 v[28:29], v[68:69], v[116:117], v[28:29] op_sel_hi:[0,1,1]
	v_pk_fma_f32 v[12:13], v[68:69], v[40:41], v[12:13] op_sel_hi:[0,1,1]
	v_pk_fma_f32 v[8:9], v[72:73], v[124:125], v[8:9] op_sel_hi:[0,1,1]
	v_pk_fma_f32 v[10:11], v[72:73], v[126:127], v[10:11] op_sel_hi:[0,1,1]
	v_pk_fma_f32 v[28:29], v[70:71], v[122:123], v[28:29] op_sel_hi:[0,1,1]
	v_pk_fma_f32 v[12:13], v[70:71], v[42:43], v[12:13] op_sel_hi:[0,1,1]
	v_pk_fma_f32 v[8:9], v[74:75], v[130:131], v[8:9] op_sel_hi:[0,1,1]
	v_pk_fma_f32 v[10:11], v[74:75], v[132:133], v[10:11] op_sel_hi:[0,1,1]
	v_pk_fma_f32 v[28:29], v[72:73], v[128:129], v[28:29] op_sel_hi:[0,1,1]
	v_pk_fma_f32 v[12:13], v[72:73], v[44:45], v[12:13] op_sel_hi:[0,1,1]
	v_pk_fma_f32 v[28:29], v[74:75], v[134:135], v[28:29] op_sel_hi:[0,1,1]
	v_pk_fma_f32 v[30:31], v[74:75], v[46:47], v[12:13] op_sel_hi:[0,1,1]
	v_mov_b32_e32 v77, v9
	v_mov_b32_e32 v12, v3
	v_mov_b32_e32 v13, v8
	v_mov_b32_e32 v5, v11
	v_mov_b32_e32 v7, v10
	v_pk_add_f32 v[12:13], v[76:77], v[12:13]
	v_pk_add_f32 v[4:5], v[4:5], v[6:7]
	v_mov_b32_e32 v57, v29
	v_mov_b32_e32 v61, v28
	v_mov_b32_e32 v65, v31
	v_mov_b32_e32 v67, v30
	v_pk_add_f32 v[4:5], v[12:13], v[4:5]
	v_pk_add_f32 v[6:7], v[56:57], v[60:61]
	v_pk_add_f32 v[12:13], v[64:65], v[66:67]
	ds_write_b128 v103, v[8:11] offset:6144
	ds_write_b128 v103, v[28:31] offset:6160
	v_pk_add_f32 v[6:7], v[6:7], v[12:13]
	s_nop 0
	v_pk_add_f32 v[4:5], v[4:5], v[6:7]
	v_mov_b32_e32 v6, 0
	v_add_f32_e32 v1, v4, v5
	s_waitcnt lgkmcnt(0)
	s_nop 1
	v_add_f32_dpp v1, v1, v1 quad_perm:[1,0,3,2] row_mask:0xf bank_mask:0xf
	s_waitcnt lgkmcnt(0)
	s_nop 1
	v_add_f32_dpp v1, v1, v1 quad_perm:[2,3,0,1] row_mask:0xf bank_mask:0xf
	s_waitcnt lgkmcnt(0)
	s_nop 1
	v_add_f32_dpp v1, v1, v1 row_half_mirror row_mask:0xf bank_mask:0xf
	s_waitcnt lgkmcnt(0)
	s_nop 1
	v_add_f32_dpp v1, v1, v1 row_mirror row_mask:0xf bank_mask:0xf
	s_waitcnt lgkmcnt(0)
	v_mov_b32_e32 v2, v1
	s_nop 1
	v_permlane16_swap_b32_e32 v2, v1
	v_add_f32_e32 v1, v1, v2
	s_waitcnt lgkmcnt(0)
	v_mov_b32_e32 v2, v1
	s_nop 1
	v_permlane32_swap_b32_e32 v2, v1
	v_add_f32_e32 v1, v1, v2
	v_mul_f32_e32 v2, 0x3a000000, v1
	v_mov_b32_e32 v1, v2
	v_mov_b32_e32 v4, v2
	v_mov_b32_e32 v5, v2
.LBB0_2911:
	v_add_u32_e32 v7, s4, v103
	ds_read_b128 v[8:11], v7
	ds_read_b128 v[28:31], v7 offset:16
	s_addk_i32 s4, 0x800
	s_cmpk_eq_i32 s4, 0x2000
	s_waitcnt lgkmcnt(1)
	v_sub_f32_e32 v12, v11, v5
	v_sub_f32_e32 v32, v9, v1
	s_waitcnt lgkmcnt(0)
	v_sub_f32_e32 v13, v31, v5
	v_sub_f32_e32 v33, v29, v1
	v_sub_f32_e32 v10, v10, v4
	v_sub_f32_e32 v8, v8, v2
	v_sub_f32_e32 v11, v30, v4
	v_sub_f32_e32 v9, v28, v2
	v_pk_mul_f32 v[28:29], v[32:33], v[32:33]
	v_pk_mul_f32 v[12:13], v[12:13], v[12:13]
	v_pk_fma_f32 v[8:9], v[8:9], v[8:9], v[28:29]
	v_pk_fma_f32 v[10:11], v[10:11], v[10:11], v[12:13]
	s_nop 0
	v_pk_add_f32 v[8:9], v[8:9], v[10:11]
	s_nop 0
	v_add_f32_e32 v7, v8, v9
	v_add_f32_e32 v6, v6, v7
	s_cbranch_scc0 .LBB0_2911
	v_mov_b64_e32 v[32:33], v[20:21]
	v_mov_b32_e32 v34, v103
	v_lshlrev_b32_e32 v172, 5, v102
	v_add_u32_e32 v172, 0x10000, v172
	s_waitcnt lgkmcnt(0)
	s_nop 1
	v_add_f32_dpp v6, v6, v6 quad_perm:[1,0,3,2] row_mask:0xf bank_mask:0xf
	s_waitcnt lgkmcnt(0)
	s_nop 1
	v_add_f32_dpp v6, v6, v6 quad_perm:[2,3,0,1] row_mask:0xf bank_mask:0xf
	s_waitcnt lgkmcnt(0)
	s_nop 1
	v_add_f32_dpp v6, v6, v6 row_half_mirror row_mask:0xf bank_mask:0xf
	s_waitcnt lgkmcnt(0)
	s_nop 1
	v_add_f32_dpp v6, v6, v6 row_mirror row_mask:0xf bank_mask:0xf
	s_waitcnt lgkmcnt(0)
	v_mov_b32_e32 v7, v6
	s_nop 1
	v_permlane16_swap_b32_e32 v7, v6
	v_add_f32_e32 v6, v6, v7
	s_waitcnt lgkmcnt(0)
	v_mov_b32_e32 v7, v6
	s_nop 1
	v_permlane32_swap_b32_e32 v7, v6
	v_add_f32_e32 v6, v6, v7
	v_fmamk_f32 v6, v6, 0x3a000000, v217
	v_cmp_gt_f32_e32 vcc, s87, v6
	v_mul_f32_e32 v7, 0x4f800000, v6
	s_nop 0
	v_cndmask_b32_e32 v6, v6, v7, vcc
	v_sqrt_f32_e32 v7, v6
	s_nop 0
	v_add_u32_e32 v8, -1, v7
	v_fma_f32 v9, -v8, v7, v6
	v_cmp_ge_f32_e64 s[4:5], 0, v9
	v_add_u32_e32 v9, 1, v7
	s_nop 0
	v_cndmask_b32_e64 v8, v7, v8, s[4:5]
	v_fma_f32 v7, -v9, v7, v6
	v_cmp_lt_f32_e64 s[4:5], 0, v7
	s_nop 1
	v_cndmask_b32_e64 v7, v8, v9, s[4:5]
	v_mul_f32_e32 v8, 0x37800000, v7
	v_cndmask_b32_e32 v7, v7, v8, vcc
	v_cmp_class_f32_e32 vcc, v6, v218
	s_nop 1
	v_cndmask_b32_e32 v6, v7, v6, vcc
	v_div_scale_f32 v7, s[4:5], v6, v6, 1.0
	v_rcp_f32_e32 v8, v7
	s_mov_b64 s[4:5], 0
	v_fma_f32 v9, -v7, v8, 1.0
	v_fmac_f32_e32 v8, v9, v8
	v_div_scale_f32 v9, vcc, 1.0, v6, 1.0
	v_mul_f32_e32 v10, v9, v8
	v_fma_f32 v11, -v7, v10, v9
	v_fmac_f32_e32 v10, v11, v8
	v_fma_f32 v7, -v7, v10, v9
	v_div_fmas_f32 v7, v7, v8, v10
	v_div_fixup_f32 v28, v7, v6, 1.0
	v_mov_b32_e32 v29, v28
	v_mov_b32_e32 v30, v28
	v_mov_b32_e32 v31, v28
	s_branch .LBB0_2915
